# speedup vs baseline: 1.0072x; 1.0057x over previous
_Z9nerf_mainPKfS0_S0_PKiS2_PKcS0_Pf:
	s_load_dwordx8 s[8:15], s[0:1], 0x20
	s_load_dwordx8 s[24:31], s[0:1], 0x0
	v_readfirstlane_b32 s3, v0
	v_and_b32_e32 v120, 63, v0
	v_lshlrev_b32_e32 v121, 4, v120
	s_getpc_b64 s[70:71]
	v_lshlrev_b32_e32 v190, 6, v0
	v_min_u32_e32 v190, 0x7700, v190
	global_load_dword v191, v190, s[70:71]
	s_mov_b32 s39, 0x20000
	s_waitcnt lgkmcnt(0)
	s_load_dword s50, s[30:31], 0x0
	s_load_dword s51, s[8:9], 0x0
	s_load_dwordx8 s[52:59], s[28:29], 0x0
	s_load_dwordx4 s[60:63], s[28:29], 0x20
	s_lshr_b32 s64, s3, 7
	s_lshl_b32 s65, s2, 2
	s_add_i32 s64, s64, s65
	s_ashr_i32 s65, s64, 31
	s_lshl_b64 s[64:65], s[64:65], 2
	s_add_u32 s66, s24, s64
	s_addc_u32 s67, s25, s65
	s_add_u32 s64, s26, s64
	s_addc_u32 s65, s27, s65
	s_load_dword s68, s[66:67], 0x0
	s_load_dword s69, s[64:65], 0x0
	v_lshlrev_b32_e32 v188, 2, v0
	v_add_u32_e32 v189, 0x1000, v188
	global_load_dword v184, v188, s[12:13]
	global_load_dword v185, v188, s[12:13] offset:2048
	global_load_dword v186, v189, s[12:13]
	global_load_dword v187, v189, s[12:13] offset:2048
	s_and_b32 s37, s11, 0xffff
	s_lshl_b32 s11, s3, 4
	s_mov_b32 s38, 0xf0000
	s_and_b32 s42, s11, 0xfffffc00
	s_mov_b32 s4, s10
	s_mov_b32 s5, s37
	s_mov_b32 s6, s38
	s_mov_b32 s7, s39
	v_or_b32_e32 v125, s42, v121
	s_add_i32 m0, s42, 0x1a000
	s_movk_i32 s11, 0x2000
	buffer_load_dwordx4 v125, s[4:7], 0 offen lds
	s_add_i32 m0, s42, 0x1c000
	s_nop 0
	buffer_load_dwordx4 v125, s[4:7], s11 offen lds
	s_add_i32 m0, s42, 0x1e000
	s_movk_i32 s11, 0x4000
	buffer_load_dwordx4 v125, s[4:7], s11 offen lds
	s_add_i32 m0, s42, 0x20000
	s_movk_i32 s11, 0x6000
	buffer_load_dwordx4 v125, s[4:7], s11 offen lds
	s_add_i32 m0, s42, 0x22000
	s_mov_b32 s11, 0xe8000
	buffer_load_dwordx4 v125, s[4:7], s11 offen lds
	s_mov_b32 s36, s10
	s_waitcnt lgkmcnt(0)
	s_mov_b32 s0, s50
	s_lshl_b32 s1, s2, 2
	s_mov_b32 s2, s51
	s_lshr_b32 s31, s3, 7
	s_bfe_u32 s30, s3, 0x10006
	s_waitcnt lgkmcnt(0)
	v_cvt_f32_i32_e32 v1, s0
	s_add_i32 s12, s31, s1
	s_add_i32 s1, s0, 0xf423f
	s_cmp_lt_u32 s1, 0x1e847f
	v_mov_b32_e32 v2, s0
	s_cselect_b64 vcc, -1, 0
	v_cndmask_b32_e32 v123, v2, v1, vcc
	v_cvt_f32_i32_e32 v1, s2
	s_add_i32 s0, s2, 0xf423f
	s_cmp_lt_u32 s0, 0x1e847f
	v_mov_b32_e32 v2, s2
	s_cselect_b64 vcc, -1, 0
	v_cndmask_b32_e32 v1, v2, v1, vcc
	v_sub_f32_e32 v122, v1, v123
	s_mov_b32 s2, 0x427c0000
	v_div_scale_f32 v1, s[0:1], s2, s2, v122
	v_rcp_f32_e32 v2, v1
	s_ashr_i32 s13, s12, 31
	s_lshl_b64 s[0:1], s[12:13], 2
	s_add_u32 s4, s24, s0
	v_fma_f32 v5, -v1, v2, 1.0
	s_addc_u32 s5, s25, s1
	v_fmac_f32_e32 v2, v5, v2
	v_div_scale_f32 v5, vcc, v122, s2, v122
	s_add_u32 s0, s26, s0
	v_mul_f32_e32 v6, v5, v2
	s_mov_b64 s[16:17], s[52:53]
	s_mov_b64 s[18:19], s[54:55]
	s_mov_b64 s[20:21], s[56:57]
	s_mov_b64 s[22:23], s[58:59]
	s_addc_u32 s1, s27, s1
	v_fma_f32 v7, -v1, v6, v5
	s_mov_b32 s4, s68
	v_fmac_f32_e32 v6, v7, v2
	s_mov_b32 s0, s69
	v_fma_f32 v1, -v1, v6, v5
	v_div_fmas_f32 v1, v1, v2, v6
	v_div_fixup_f32 v124, v1, s2, v122
	s_waitcnt lgkmcnt(0)
	v_mov_b32_e32 v1, s16
	s_mov_b64 s[24:25], s[60:61]
	s_mov_b64 s[26:27], s[62:63]
	v_mul_f32_e32 v1, s4, v1
	v_mov_b32_e32 v2, s0
	v_fma_f32 v1, s17, -v2, v1
	v_add_f32_e32 v127, s19, v1
	v_mov_b32_e32 v1, s20
	v_mul_f32_e32 v1, s4, v1
	v_fma_f32 v1, s21, -v2, v1
	v_add_f32_e32 v128, s23, v1
	s_waitcnt lgkmcnt(0)
	v_mov_b32_e32 v1, s24
	v_mul_f32_e32 v1, s4, v1
	v_and_b32_e32 v3, 15, v0
	v_fma_f32 v1, s25, -v2, v1
	v_and_b32_e32 v131, 48, v0
	v_lshl_or_b32 v0, s30, 6, v120
	v_add_f32_e32 v129, s27, v1
	v_add_u32_e32 v1, 1, v0
	v_cvt_f32_ubyte0_e32 v1, v1
	s_mov_b32 s4, 0x43010000
	s_and_b32 s19, s3, 0xffffff80
	v_div_scale_f32 v2, s[2:3], s4, s4, v1
	v_lshl_or_b32 v130, s30, 5, v3
	v_rcp_f32_e32 v3, v2
	v_lshrrev_b32_e32 v4, 4, v120
	v_cmp_eq_u32_e64 s[8:9], 2, v4
	v_cmp_eq_u32_e64 s[10:11], 1, v4
	v_fma_f32 v5, -v2, v3, 1.0
	v_fmac_f32_e32 v3, v5, v3
	v_div_scale_f32 v5, vcc, v1, s4, v1
	v_mul_f32_e32 v6, v5, v3
	v_fma_f32 v7, -v2, v6, v5
	v_fmac_f32_e32 v6, v7, v3
	v_fma_f32 v2, -v2, v6, v5
	v_div_fmas_f32 v2, v2, v3, v6
	v_div_fixup_f32 v134, v2, s4, v1
	v_add_u32_e32 v2, -1, v4
	v_cmp_gt_u32_e32 vcc, 2, v2
	v_mov_b32_e32 v2, 0x401550d3
	v_mov_b32_e32 v3, 0x436d0620
	v_cndmask_b32_e64 v5, v2, v3, s[8:9]
	v_mov_b32_e32 v6, 0x412e2e5e
	v_cmp_eq_u32_e64 s[0:1], 3, v4
	v_cndmask_b32_e64 v4, v5, v6, s[10:11]
	v_cmp_gt_u32_e64 s[2:3], 16, v120
	v_bfrev_b32_e32 v5, 34
	v_mov_b32_e32 v8, 0x41bc2043
	v_cndmask_b32_e64 v140, v4, 0.5, s[2:3]
	v_mov_b32_e32 v4, 0x40a14518
	v_cndmask_b32_e64 v7, v4, v5, s[8:9]
	v_cndmask_b32_e64 v7, v7, v8, s[10:11]
	v_mov_b32_e32 v9, 0x3f8a3f66
	v_cndmask_b32_e64 v141, v7, v9, s[2:3]
	v_cndmask_b32_e64 v7, v6, 0.5, s[8:9]
	v_cndmask_b32_e64 v6, v3, v6, s[8:9]
	v_mov_b32_e32 v10, 0x424b2ff5
	v_cndmask_b32_e64 v6, v6, 0.5, s[10:11]
	v_cndmask_b32_e64 v144, v6, v10, s[2:3]
	v_cndmask_b32_e64 v6, v5, v8, s[8:9]
	v_or_b32_e32 v0, s19, v0
	v_mov_b32_e32 v11, 0x42db7457
	v_cndmask_b32_e64 v6, v6, v9, s[10:11]
	v_lshlrev_b32_e32 v0, 2, v0
	v_cndmask_b32_e64 v7, v7, v10, s[10:11]
	v_cndmask_b32_e64 v145, v6, v11, s[2:3]
	v_cndmask_b32_e64 v6, 0, v10, s[8:9]
	v_add_u32_e32 v135, 0x15000, v0
	v_add_u32_e32 v136, 0x15800, v0
	v_cvt_f32_ubyte0_e32 v0, v130
	v_or_b32_e32 v138, 16, v130
	v_cndmask_b32_e64 v142, v7, v2, s[2:3]
	v_cndmask_b32_e64 v2, v6, v2, s[10:11]
	s_lshl_b32 s13, s31, 10
	s_lshl_b32 s44, s31, 8
	v_fma_f32 v137, v0, v124, v123
	v_cvt_f32_ubyte0_e32 v0, v138
	v_cndmask_b32_e64 v7, v8, v9, s[8:9]
	v_cndmask_b32_e64 v146, v2, v3, s[2:3]
	v_cndmask_b32_e64 v2, 0, v11, s[8:9]
	s_lshl_b32 s27, s19, 2
	s_add_i32 s13, s13, 0x12000
	s_add_i32 s44, s44, 0x16000
	v_fma_f32 v139, v0, v124, v123
	v_lshlrev_b32_e32 v0, 4, v130
	v_lshlrev_b32_e32 v1, 4, v138
	v_cndmask_b32_e64 v7, v7, v11, s[10:11]
	v_cndmask_b32_e64 v2, v2, v4, s[10:11]
	v_or_b32_e32 v126, 0x2000, v121
	s_add_i32 s23, s27, 0x15000
	s_add_i32 s28, s42, 0xa000
	s_add_i32 s29, s42, 0xc000
	s_add_i32 s33, s42, 0xe000
	s_add_i32 s34, s42, 0x10000
	s_add_i32 s35, s42, 0x2000
	s_add_i32 s40, s42, 0x8000
	s_add_i32 s41, s42, 0x6000
	s_addk_i32 s42, 0x4000
	s_sub_i32 s43, s19, 64
	v_lshl_or_b32 v132, v120, 4, s13
	v_lshl_or_b32 v133, v120, 2, s44
	s_mov_b32 s20, 1
	s_or_b64 s[4:5], s[2:3], vcc
	s_or_b64 s[6:7], s[2:3], s[10:11]
	v_cndmask_b32_e64 v143, v7, v4, s[2:3]
	s_mov_b32 s45, 0
	v_cndmask_b32_e64 v147, v2, v5, s[2:3]
	v_or_b32_e32 v148, 0x1a000, v121
	v_or_b32_e32 v149, 0x1a400, v121
	v_or_b32_e32 v150, 0x1a800, v121
	v_or_b32_e32 v151, 0x1ac00, v121
	v_or_b32_e32 v152, 0x1b000, v121
	v_or_b32_e32 v153, 0x1b400, v121
	v_or_b32_e32 v154, 0x1b800, v121
	v_or_b32_e32 v155, 0x1bc00, v121
	v_or_b32_e32 v156, 0x1c000, v121
	v_or_b32_e32 v157, 0x1c400, v121
	v_or_b32_e32 v158, 0x1c800, v121
	v_or_b32_e32 v159, 0x1cc00, v121
	v_or_b32_e32 v160, 0x1d000, v121
	v_or_b32_e32 v161, 0x1d400, v121
	v_or_b32_e32 v162, 0x1d800, v121
	v_or_b32_e32 v163, 0x1dc00, v121
	v_or_b32_e32 v164, 0x1e000, v121
	v_or_b32_e32 v165, 0x1e400, v121
	v_or_b32_e32 v166, 0x1e800, v121
	v_or_b32_e32 v167, 0x1ec00, v121
	v_or_b32_e32 v168, 0x1f000, v121
	v_or_b32_e32 v169, 0x1f400, v121
	v_or_b32_e32 v170, 0x1f800, v121
	v_or_b32_e32 v171, 0x1fc00, v121
	v_or_b32_e32 v172, 0x20000, v121
	v_or_b32_e32 v173, 0x20400, v121
	v_or_b32_e32 v174, 0x20800, v121
	v_or_b32_e32 v175, 0x20c00, v121
	v_or_b32_e32 v176, 0x21000, v121
	v_or_b32_e32 v177, 0x21400, v121
	v_or_b32_e32 v178, 0x21800, v121
	v_or_b32_e32 v179, 0x21c00, v121
	v_add_u32_e32 v180, s13, v0
	v_add_u32_e32 v181, s13, v1
	v_mov_b32_e32 v182, 0x13000
	s_waitcnt vmcnt(5)
	ds_write_b32 v188, v184
	ds_write_b32 v188, v185 offset:2048
	ds_write_b32 v188, v186 offset:4096
	ds_write_b32 v188, v187 offset:6144
	s_branch .LBB1_5
